# speedup vs baseline: 1.0069x; 1.0023x over previous
.LBB1_9:
	s_xor_b64 s[30:31], s[20:21], -1
	s_waitcnt lgkmcnt(14)
	v_mfma_f32_32x32x16_f16 v[18:33], v[128:131], v[172:175], v[18:33]
	v_exp_f32_e32 v66, v66
	v_exp_f32_e32 v67, v67
	v_exp_f32_e32 v68, v68
	v_exp_f32_e32 v69, v69
	s_waitcnt lgkmcnt(12)
	v_mfma_f32_32x32x16_f16 v[2:17], v[128:131], v[176:179], v[2:17]
	v_exp_f32_e32 v70, v70
	v_exp_f32_e32 v71, v71
	v_exp_f32_e32 v72, v72
	v_exp_f32_e32 v73, v73
	v_add_u32_e32 v54, s45, v217
	v_add_u32_e32 v55, v54, v207
	ds_read_b128 v[50:53], v55
	ds_read_b128 v[34:37], v55 offset:4096
	s_waitcnt lgkmcnt(12)
	v_mfma_f32_32x32x16_f16 v[18:33], v[106:109], v[122:125], v[18:33]
	v_exp_f32_e32 v74, v74
	v_exp_f32_e32 v75, v75
	v_exp_f32_e32 v76, v76
	v_exp_f32_e32 v77, v77
	v_add_u32_e32 v55, v54, v206
	ds_read_b128 v[122:125], v55
	ds_read_b128 v[172:175], v55 offset:4096
	s_waitcnt lgkmcnt(12)
	v_mfma_f32_32x32x16_f16 v[2:17], v[106:109], v[118:121], v[2:17]
	v_exp_f32_e32 v78, v78
	v_exp_f32_e32 v79, v79
	v_exp_f32_e32 v80, v80
	v_exp_f32_e32 v81, v81
	v_add_u32_e32 v55, v54, v205
	ds_read_b128 v[176:179], v55
	ds_read_b128 v[164:167], v55 offset:4096
	s_waitcnt lgkmcnt(12)
	v_mfma_f32_32x32x16_f16 v[18:33], v[102:105], v[114:117], v[18:33]
	v_exp_f32_e32 v82, v82
	v_exp_f32_e32 v83, v83
	v_exp_f32_e32 v84, v84
	v_exp_f32_e32 v85, v85
	v_add_u32_e32 v54, v54, v204
	ds_read_b128 v[168:171], v54
	ds_read_b128 v[160:163], v54 offset:4096
	s_waitcnt lgkmcnt(12)
	v_mfma_f32_32x32x16_f16 v[2:17], v[102:105], v[110:113], v[2:17]
	v_exp_f32_e32 v86, v86
	v_exp_f32_e32 v87, v87
	v_exp_f32_e32 v88, v88
	v_exp_f32_e32 v89, v89
	s_waitcnt lgkmcnt(10)
	v_mfma_f32_32x32x16_f16 v[18:33], v[98:101], v[156:159], v[18:33]
	v_exp_f32_e32 v90, v90
	v_exp_f32_e32 v91, v91
	v_exp_f32_e32 v92, v92
	v_exp_f32_e32 v93, v93
	s_waitcnt lgkmcnt(8)
	v_mfma_f32_32x32x16_f16 v[2:17], v[98:101], v[152:155], v[2:17]
	v_exp_f32_e32 v94, v94
	v_exp_f32_e32 v95, v95
	v_exp_f32_e32 v96, v96
	v_exp_f32_e32 v97, v97
	s_waitcnt vmcnt(4) lgkmcnt(0)
	s_barrier
	s_cmp_lg_u32 s37, 0
	s_cbranch_scc1 .Lstag_2
	s_sleep 3
.Lstag_2:
	s_andn2_b64 vcc, exec, s[2:3]
	s_cbranch_vccnz .LBB1_11
	ds_read_b128 v[54:57], v213 offset:96
	ds_read_b128 v[58:61], v213 offset:64
	ds_read_b128 v[62:65], v213 offset:32
	ds_read_b128 v[38:41], v213
	s_waitcnt lgkmcnt(3)
	v_pk_mul_f32 v[32:33], v[32:33], v[56:57]
	s_waitcnt lgkmcnt(2)
	v_pk_mul_f32 v[28:29], v[28:29], v[60:61]
	s_waitcnt lgkmcnt(1)
	v_pk_mul_f32 v[24:25], v[24:25], v[64:65]
	s_waitcnt lgkmcnt(0)
	v_pk_mul_f32 v[20:21], v[20:21], v[40:41]
	v_pk_mul_f32 v[30:31], v[30:31], v[54:55]
	v_pk_mul_f32 v[26:27], v[26:27], v[58:59]
	v_pk_mul_f32 v[22:23], v[22:23], v[62:63]
	v_pk_mul_f32 v[18:19], v[18:19], v[38:39]
	v_pk_mul_f32 v[16:17], v[16:17], v[56:57]
	v_pk_mul_f32 v[12:13], v[12:13], v[60:61]
	v_pk_mul_f32 v[8:9], v[8:9], v[64:65]
	v_pk_mul_f32 v[4:5], v[4:5], v[40:41]
	v_pk_mul_f32 v[14:15], v[14:15], v[54:55]
	v_pk_mul_f32 v[10:11], v[10:11], v[58:59]
	v_pk_mul_f32 v[6:7], v[6:7], v[62:63]
	v_pk_mul_f32 v[2:3], v[2:3], v[38:39]

.LBB1_16:
	s_waitcnt lgkmcnt(14)
	v_mfma_f32_32x32x16_f16 v[18:33], v[128:131], v[118:121], v[18:33]
	v_exp_f32_e32 v50, v50
	v_exp_f32_e32 v51, v51
	v_exp_f32_e32 v52, v52
	v_exp_f32_e32 v53, v53
	s_waitcnt lgkmcnt(12)
	v_mfma_f32_32x32x16_f16 v[2:17], v[128:131], v[152:155], v[2:17]
	v_exp_f32_e32 v54, v54
	v_exp_f32_e32 v55, v55
	v_exp_f32_e32 v56, v56
	v_exp_f32_e32 v57, v57
	v_add_u32_e32 v70, s43, v217
	v_add_u32_e32 v71, v70, v207
	ds_read_b128 v[66:69], v71
	ds_read_b128 v[82:85], v71 offset:4096
	s_waitcnt lgkmcnt(12)
	v_mfma_f32_32x32x16_f16 v[18:33], v[106:109], v[148:151], v[18:33]
	v_exp_f32_e32 v58, v58
	v_exp_f32_e32 v59, v59
	v_exp_f32_e32 v60, v60
	v_exp_f32_e32 v61, v61
	v_add_u32_e32 v71, v70, v206
	ds_read_b128 v[168:171], v71
	ds_read_b128 v[164:167], v71 offset:4096
	s_waitcnt lgkmcnt(12)
	v_mfma_f32_32x32x16_f16 v[2:17], v[106:109], v[122:125], v[2:17]
	v_exp_f32_e32 v62, v62
	v_exp_f32_e32 v63, v63
	v_exp_f32_e32 v64, v64
	v_exp_f32_e32 v65, v65
	v_add_u32_e32 v71, v70, v205
	ds_read_b128 v[160:163], v71
	ds_read_b128 v[156:159], v71 offset:4096
	s_waitcnt lgkmcnt(12)
	v_mfma_f32_32x32x16_f16 v[18:33], v[102:105], v[114:117], v[18:33]
	v_exp_f32_e32 v34, v34
	v_exp_f32_e32 v35, v35
	v_exp_f32_e32 v36, v36
	v_exp_f32_e32 v37, v37
	v_add_u32_e32 v70, v70, v204
	ds_read_b128 v[152:155], v70
	ds_read_b128 v[148:151], v70 offset:4096
	s_waitcnt lgkmcnt(12)
	v_mfma_f32_32x32x16_f16 v[2:17], v[102:105], v[110:113], v[2:17]
	v_exp_f32_e32 v38, v38
	v_exp_f32_e32 v39, v39
	v_exp_f32_e32 v40, v40
	v_exp_f32_e32 v41, v41
	s_waitcnt lgkmcnt(10)
	v_mfma_f32_32x32x16_f16 v[18:33], v[98:101], v[172:175], v[18:33]
	v_exp_f32_e32 v42, v42
	v_exp_f32_e32 v43, v43
	v_exp_f32_e32 v44, v44
	v_exp_f32_e32 v45, v45
	s_waitcnt lgkmcnt(8)
	v_mfma_f32_32x32x16_f16 v[2:17], v[98:101], v[176:179], v[2:17]
	v_exp_f32_e32 v46, v46
	v_exp_f32_e32 v47, v47
	v_exp_f32_e32 v48, v48
	v_exp_f32_e32 v49, v49
	s_waitcnt vmcnt(4) lgkmcnt(0)
	s_barrier
	s_cmp_lg_u32 s37, 0
	s_cbranch_scc1 .Lstag_1
	s_sleep 3
.Lstag_1:
	s_andn2_b64 vcc, exec, s[30:31]
	s_cbranch_vccnz .LBB1_18
	ds_read_b128 v[70:73], v213 offset:96
	ds_read_b128 v[74:77], v213 offset:64
	ds_read_b128 v[78:81], v213 offset:32
	ds_read_b128 v[86:89], v213
	s_waitcnt lgkmcnt(3)
	v_pk_mul_f32 v[32:33], v[32:33], v[72:73]
	s_waitcnt lgkmcnt(2)
	v_pk_mul_f32 v[28:29], v[28:29], v[76:77]
	s_waitcnt lgkmcnt(1)
	v_pk_mul_f32 v[24:25], v[24:25], v[80:81]
	s_waitcnt lgkmcnt(0)
	v_pk_mul_f32 v[20:21], v[20:21], v[88:89]
	v_pk_mul_f32 v[30:31], v[30:31], v[70:71]
	v_pk_mul_f32 v[26:27], v[26:27], v[74:75]
	v_pk_mul_f32 v[22:23], v[22:23], v[78:79]
	v_pk_mul_f32 v[18:19], v[18:19], v[86:87]
	v_pk_mul_f32 v[16:17], v[16:17], v[72:73]
	v_pk_mul_f32 v[12:13], v[12:13], v[76:77]
	v_pk_mul_f32 v[8:9], v[8:9], v[80:81]
	v_pk_mul_f32 v[4:5], v[4:5], v[88:89]
	v_pk_mul_f32 v[14:15], v[14:15], v[70:71]
	v_pk_mul_f32 v[10:11], v[10:11], v[74:75]
	v_pk_mul_f32 v[6:7], v[6:7], v[78:79]
	v_pk_mul_f32 v[2:3], v[2:3], v[86:87]

.LBB1_135:
	v_mov_b32_e32 v32, 0xff800000
	v_cmp_neq_f32_e32 vcc, 0, v80
	s_nop 1
	v_cndmask_b32_e32 v80, v32, v80, vcc
	v_cmp_neq_f32_e32 vcc, 0, v96
	s_nop 1
	v_cndmask_b32_e32 v96, v32, v96, vcc
	v_cmp_neq_f32_e32 vcc, 0, v81
	s_nop 1
	v_cndmask_b32_e32 v81, v32, v81, vcc
	v_cmp_neq_f32_e32 vcc, 0, v97
	s_nop 1
	v_cndmask_b32_e32 v97, v32, v97, vcc
	v_cmp_neq_f32_e32 vcc, 0, v82
	s_nop 1
	v_cndmask_b32_e32 v82, v32, v82, vcc
	v_cmp_neq_f32_e32 vcc, 0, v98
	s_nop 1
	v_cndmask_b32_e32 v98, v32, v98, vcc
	v_cmp_neq_f32_e32 vcc, 0, v83
	s_nop 1
	v_cndmask_b32_e32 v83, v32, v83, vcc
	v_cmp_neq_f32_e32 vcc, 0, v99
	s_nop 1
	v_cndmask_b32_e32 v99, v32, v99, vcc
	v_cmp_neq_f32_e32 vcc, 0, v84
	s_nop 1
	v_cndmask_b32_e32 v84, v32, v84, vcc
	v_cmp_neq_f32_e32 vcc, 0, v100
	s_nop 1
	v_cndmask_b32_e32 v100, v32, v100, vcc
	v_cmp_neq_f32_e32 vcc, 0, v85
	s_nop 1
	v_cndmask_b32_e32 v85, v32, v85, vcc
	v_cmp_neq_f32_e32 vcc, 0, v101
	s_nop 1
	v_cndmask_b32_e32 v101, v32, v101, vcc
	v_cmp_neq_f32_e32 vcc, 0, v86
	s_nop 1
	v_cndmask_b32_e32 v86, v32, v86, vcc
	v_cmp_neq_f32_e32 vcc, 0, v102
	s_nop 1
	v_cndmask_b32_e32 v102, v32, v102, vcc
	v_cmp_neq_f32_e32 vcc, 0, v87
	s_nop 1
	v_cndmask_b32_e32 v87, v32, v87, vcc
	v_cmp_neq_f32_e32 vcc, 0, v103
	s_nop 1
	v_cndmask_b32_e32 v103, v32, v103, vcc
	v_cmp_neq_f32_e32 vcc, 0, v88
	s_nop 1
	v_cndmask_b32_e32 v88, v32, v88, vcc
	v_cmp_neq_f32_e32 vcc, 0, v104
	s_nop 1
	v_cndmask_b32_e32 v104, v32, v104, vcc
	v_cmp_neq_f32_e32 vcc, 0, v89
	s_nop 1
	v_cndmask_b32_e32 v89, v32, v89, vcc
	v_cmp_neq_f32_e32 vcc, 0, v105
	s_nop 1
	v_cndmask_b32_e32 v105, v32, v105, vcc
	v_cmp_neq_f32_e32 vcc, 0, v90
	s_nop 1
	v_cndmask_b32_e32 v90, v32, v90, vcc
	v_cmp_neq_f32_e32 vcc, 0, v106
	s_nop 1
	v_cndmask_b32_e32 v106, v32, v106, vcc
	v_cmp_neq_f32_e32 vcc, 0, v91
	s_nop 1
	v_cndmask_b32_e32 v91, v32, v91, vcc
	v_cmp_neq_f32_e32 vcc, 0, v107
	s_nop 1
	v_cndmask_b32_e32 v107, v32, v107, vcc
	v_cmp_neq_f32_e32 vcc, 0, v92
	s_nop 1
	v_cndmask_b32_e32 v92, v32, v92, vcc
	v_cmp_neq_f32_e32 vcc, 0, v108
	s_nop 1
	v_cndmask_b32_e32 v108, v32, v108, vcc
	v_cmp_neq_f32_e32 vcc, 0, v93
	s_nop 1
	v_cndmask_b32_e32 v93, v32, v93, vcc
	v_cmp_neq_f32_e32 vcc, 0, v109
	s_nop 1
	v_cndmask_b32_e32 v109, v32, v109, vcc
	v_cmp_neq_f32_e32 vcc, 0, v94
	s_nop 1
	v_cndmask_b32_e32 v94, v32, v94, vcc
	v_cmp_neq_f32_e32 vcc, 0, v110
	s_nop 1
	v_cndmask_b32_e32 v110, v32, v110, vcc
	v_cmp_neq_f32_e32 vcc, 0, v95
	s_nop 1
	v_cndmask_b32_e32 v95, v32, v95, vcc
	v_cmp_neq_f32_e32 vcc, 0, v111
	s_nop 1
	v_cndmask_b32_e32 v111, v32, v111, vcc
	s_branch .LBB1_93
	s_nop 0
	s_nop 0
	s_nop 0
	s_nop 0
	s_nop 0
	s_nop 0
	s_nop 0
	s_nop 0
	s_nop 0
	s_nop 0
	s_nop 0
	s_nop 0
	s_nop 0
	s_nop 0
	s_nop 0
	s_nop 0
	s_nop 0
	s_nop 0
	s_nop 0
	s_nop 0
	s_nop 0
	s_nop 0
	s_nop 0
	s_nop 0
	s_nop 0
	s_endpgm
